# baseline (speedup 1.0000x reference)
_Z16rec_chunk_kernelPKDF16_PKfS2_S2_PfS3_:
	s_load_dwordx4 s[12:15], s[0:1], 0x0
	s_cmpk_lt_u32 s2, 0xc0
	s_mov_b64 s[4:5], -1
	s_cbranch_scc0 .LBB2_4
	s_load_dwordx8 s[4:11], s[0:1], 0x10
	s_and_b32 s36, s2, 7
	s_lshr_b32 s37, s2, 3
	s_mul_i32 s38, s37, 43
	s_lshr_b32 s38, s38, 8
	s_mul_i32 s39, s38, 6
	s_sub_i32 s39, s37, s39
	s_lshl_b32 s36, s36, 2
	s_add_i32 s36, s36, s38
	s_mul_i32 s48, s36, 0x54000
	s_mul_i32 s49, s36, 48
	s_add_i32 s49, s49, s39
	s_lshl_b32 s49, s49, 13
	s_lshr_b32 s50, s36, 3
	s_and_b32 s51, s36, 7
	s_mul_i32 s50, s50, 0x9c000
	s_mul_i32 s51, s51, 0x12000
	s_add_i32 s50, s50, s51
	s_lshl_b32 s51, s39, 7
	s_add_i32 s50, s50, s51
	v_lshlrev_b32_e32 v1, 4, v0
	v_lshrrev_b32_e32 v170, 5, v0
	v_and_b32_e32 v171, 31, v0
	v_mul_u32_u24_e32 v170, 0xc00, v170
	v_lshl_add_u32 v170, v171, 2, v170
	s_waitcnt lgkmcnt(0)
	s_mov_b32 s16, s12
	s_and_b32 s17, s13, 0xffff
	s_mov_b32 s18, 0xa80000
	s_mov_b32 s19, 0x20000
	s_mov_b32 s20, s14
	s_and_b32 s21, s15, 0xffff
	s_mov_b32 s22, 0xc00000
	s_mov_b32 s23, 0x20000
	s_mov_b32 s24, s8
	s_and_b32 s25, s9, 0xffff
	s_mov_b32 s26, 0xc00000
	s_mov_b32 s27, 0x20000
	s_mov_b32 s28, s6
	s_and_b32 s29, s7, 0xffff
	s_mov_b32 s30, 0x270000
	s_mov_b32 s31, 0x20000
	s_mov_b32 s32, s10
	s_and_b32 s33, s11, 0xffff
	s_mov_b32 s34, 0x270000
	s_mov_b32 s35, 0x20000
	s_lshl_b32 s52, s36, 5
	s_add_u32 s52, s4, s52
	s_addc_u32 s53, s5, 0
	s_load_dwordx8 s[40:47], s[52:53], 0x0
	s_add_i32 s56, s50, 0
	buffer_load_dword v2, v170, s[28:31], s56 offen
	buffer_load_dword v3, v170, s[28:31], s56 offen offset:768
	buffer_load_dword v4, v170, s[28:31], s56 offen offset:1536
	buffer_load_dword v5, v170, s[28:31], s56 offen offset:2304
	s_add_i32 s56, s50, 6144
	buffer_load_dword v6, v170, s[28:31], s56 offen
	buffer_load_dword v7, v170, s[28:31], s56 offen offset:768
	buffer_load_dword v8, v170, s[28:31], s56 offen offset:1536
	buffer_load_dword v9, v170, s[28:31], s56 offen offset:2304
	s_add_i32 s56, s50, 12288
	buffer_load_dword v10, v170, s[28:31], s56 offen
	buffer_load_dword v11, v170, s[28:31], s56 offen offset:768
	buffer_load_dword v12, v170, s[28:31], s56 offen offset:1536
	buffer_load_dword v13, v170, s[28:31], s56 offen offset:2304
	s_add_i32 s56, s50, 18432
	buffer_load_dword v14, v170, s[28:31], s56 offen
	buffer_load_dword v15, v170, s[28:31], s56 offen offset:768
	buffer_load_dword v16, v170, s[28:31], s56 offen offset:1536
	buffer_load_dword v17, v170, s[28:31], s56 offen offset:2304
	s_add_i32 s56, s50, 24576
	buffer_load_dword v18, v170, s[28:31], s56 offen
	buffer_load_dword v19, v170, s[28:31], s56 offen offset:768
	buffer_load_dword v20, v170, s[28:31], s56 offen offset:1536
	buffer_load_dword v21, v170, s[28:31], s56 offen offset:2304
	s_add_i32 s56, s50, 30720
	buffer_load_dword v22, v170, s[28:31], s56 offen
	buffer_load_dword v23, v170, s[28:31], s56 offen offset:768
	buffer_load_dword v24, v170, s[28:31], s56 offen offset:1536
	buffer_load_dword v25, v170, s[28:31], s56 offen offset:2304
	s_add_i32 s56, s50, 36864
	buffer_load_dword v26, v170, s[28:31], s56 offen
	buffer_load_dword v27, v170, s[28:31], s56 offen offset:768
	buffer_load_dword v28, v170, s[28:31], s56 offen offset:1536
	buffer_load_dword v29, v170, s[28:31], s56 offen offset:2304
	s_add_i32 s56, s50, 43008
	buffer_load_dword v30, v170, s[28:31], s56 offen
	buffer_load_dword v31, v170, s[28:31], s56 offen offset:768
	buffer_load_dword v32, v170, s[28:31], s56 offen offset:1536
	buffer_load_dword v33, v170, s[28:31], s56 offen offset:2304
	s_add_i32 s56, s50, 49152
	buffer_load_dword v34, v170, s[28:31], s56 offen
	buffer_load_dword v35, v170, s[28:31], s56 offen offset:768
	buffer_load_dword v36, v170, s[28:31], s56 offen offset:1536
	buffer_load_dword v37, v170, s[28:31], s56 offen offset:2304
	s_add_i32 s56, s50, 55296
	buffer_load_dword v38, v170, s[28:31], s56 offen
	buffer_load_dword v39, v170, s[28:31], s56 offen offset:768
	buffer_load_dword v40, v170, s[28:31], s56 offen offset:1536
	buffer_load_dword v41, v170, s[28:31], s56 offen offset:2304
	s_add_i32 s56, s50, 61440
	buffer_load_dword v42, v170, s[28:31], s56 offen
	buffer_load_dword v43, v170, s[28:31], s56 offen offset:768
	buffer_load_dword v44, v170, s[28:31], s56 offen offset:1536
	buffer_load_dword v45, v170, s[28:31], s56 offen offset:2304
	s_add_i32 s56, s50, 67584
	buffer_load_dword v46, v170, s[28:31], s56 offen
	buffer_load_dword v47, v170, s[28:31], s56 offen offset:768
	buffer_load_dword v48, v170, s[28:31], s56 offen offset:1536
	buffer_load_dword v49, v170, s[28:31], s56 offen offset:2304
	s_mov_b32 s60, s48
	s_mov_b32 s61, s49
	s_add_i32 s56, s60, 0
	buffer_load_dwordx4 a[0:3], v1, s[16:19], s56 offen
	s_add_i32 s57, s60, 6144
	buffer_load_dwordx4 a[4:7], v1, s[16:19], s57 offen
	s_add_i32 s56, s60, 12288
	buffer_load_dwordx4 a[8:11], v1, s[16:19], s56 offen
	s_add_i32 s57, s60, 18432
	buffer_load_dwordx4 a[12:15], v1, s[16:19], s57 offen
	s_add_i32 s56, s60, 1024
	buffer_load_dwordx4 a[16:19], v1, s[16:19], s56 offen
	s_add_i32 s57, s60, 7168
	buffer_load_dwordx4 a[20:23], v1, s[16:19], s57 offen
	s_add_i32 s56, s60, 13312
	buffer_load_dwordx4 a[24:27], v1, s[16:19], s56 offen
	s_add_i32 s57, s60, 19456
	buffer_load_dwordx4 a[28:31], v1, s[16:19], s57 offen
	s_add_i32 s58, s61, 0
	buffer_load_dwordx4 v[114:117], v1, s[20:23], s58 offen
	s_add_i32 s59, s61, 1024
	buffer_load_dwordx4 v[118:121], v1, s[20:23], s59 offen
	s_add_i32 s58, s61, 2048
	buffer_load_dwordx4 v[122:125], v1, s[20:23], s58 offen
	s_add_i32 s59, s61, 3072
	buffer_load_dwordx4 v[126:129], v1, s[20:23], s59 offen
	s_add_i32 s58, s61, 4096
	buffer_load_dwordx4 v[130:133], v1, s[20:23], s58 offen
	s_add_i32 s59, s61, 5120
	buffer_load_dwordx4 v[134:137], v1, s[20:23], s59 offen
	s_add_i32 s58, s61, 6144
	buffer_load_dwordx4 v[138:141], v1, s[20:23], s58 offen
	s_add_i32 s59, s61, 7168
	buffer_load_dwordx4 v[142:145], v1, s[20:23], s59 offen
	s_add_i32 s56, s60, 2048
	buffer_load_dwordx4 a[32:35], v1, s[16:19], s56 offen
	s_add_i32 s57, s60, 8192
	buffer_load_dwordx4 a[36:39], v1, s[16:19], s57 offen
	s_add_i32 s56, s60, 14336
	buffer_load_dwordx4 a[40:43], v1, s[16:19], s56 offen
	s_add_i32 s57, s60, 20480
	buffer_load_dwordx4 a[44:47], v1, s[16:19], s57 offen
	s_add_i32 s56, s60, 3072
	buffer_load_dwordx4 a[48:51], v1, s[16:19], s56 offen
	s_add_i32 s57, s60, 9216
	buffer_load_dwordx4 a[52:55], v1, s[16:19], s57 offen
	s_add_i32 s56, s60, 15360
	buffer_load_dwordx4 a[56:59], v1, s[16:19], s56 offen
	s_add_i32 s57, s60, 21504
	buffer_load_dwordx4 a[60:63], v1, s[16:19], s57 offen
	s_add_i32 s56, s60, 4096
	buffer_load_dwordx4 a[64:67], v1, s[16:19], s56 offen
	s_add_i32 s57, s60, 10240
	buffer_load_dwordx4 a[68:71], v1, s[16:19], s57 offen
	s_add_i32 s56, s60, 16384
	buffer_load_dwordx4 a[72:75], v1, s[16:19], s56 offen
	s_add_i32 s57, s60, 22528
	buffer_load_dwordx4 a[76:79], v1, s[16:19], s57 offen
	s_add_i32 s56, s60, 5120
	buffer_load_dwordx4 a[80:83], v1, s[16:19], s56 offen
	s_add_i32 s57, s60, 11264
	buffer_load_dwordx4 a[84:87], v1, s[16:19], s57 offen
	s_add_i32 s56, s60, 17408
	buffer_load_dwordx4 a[88:91], v1, s[16:19], s56 offen
	s_add_i32 s57, s60, 23552
	buffer_load_dwordx4 a[92:95], v1, s[16:19], s57 offen
	s_add_i32 s56, s60, 30720
	buffer_load_dwordx4 a[96:99], v1, s[16:19], s56 offen
	s_add_i32 s57, s60, 34816
	buffer_load_dwordx4 a[100:103], v1, s[16:19], s57 offen
	s_add_i32 s56, s60, 38912
	buffer_load_dwordx4 a[104:107], v1, s[16:19], s56 offen
	s_add_i32 s57, s60, 24576
	buffer_load_dwordx4 a[108:111], v1, s[16:19], s57 offen
	s_add_i32 s56, s60, 26624
	buffer_load_dwordx4 a[112:115], v1, s[16:19], s56 offen
	s_add_i32 s56, s60, 31744
	buffer_load_dwordx4 a[116:119], v1, s[16:19], s56 offen
	s_add_i32 s57, s60, 35840
	buffer_load_dwordx4 a[120:123], v1, s[16:19], s57 offen
	s_add_i32 s56, s60, 39936
	buffer_load_dwordx4 a[124:127], v1, s[16:19], s56 offen
	s_add_i32 s57, s60, 25600
	buffer_load_dwordx4 a[128:131], v1, s[16:19], s57 offen
	s_add_i32 s56, s60, 27648
	buffer_load_dwordx4 a[132:135], v1, s[16:19], s56 offen
	s_add_i32 s56, s60, 32768
	buffer_load_dwordx4 a[136:139], v1, s[16:19], s56 offen
	s_add_i32 s57, s60, 36864
	buffer_load_dwordx4 a[140:143], v1, s[16:19], s57 offen
	s_add_i32 s56, s60, 40960
	buffer_load_dwordx4 a[144:147], v1, s[16:19], s56 offen
	s_add_i32 s57, s60, 28672
	buffer_load_dwordx4 a[148:151], v1, s[16:19], s57 offen
	s_add_i32 s56, s60, 33792
	buffer_load_dwordx4 a[152:155], v1, s[16:19], s56 offen
	s_add_i32 s57, s60, 37888
	buffer_load_dwordx4 a[156:159], v1, s[16:19], s57 offen
	s_add_i32 s56, s60, 41984
	buffer_load_dwordx4 a[160:163], v1, s[16:19], s56 offen
	s_add_i32 s57, s60, 29696
	buffer_load_dwordx4 a[164:167], v1, s[16:19], s57 offen
	buffer_load_dword v171, v1, s[20:23], s49 offen
	buffer_load_dword v171, v1, s[20:23], s49 offen
	buffer_load_dword v171, v1, s[20:23], s49 offen
	buffer_load_dword v171, v1, s[20:23], s49 offen
	buffer_load_dword v171, v1, s[20:23], s49 offen
	buffer_load_dword v171, v1, s[20:23], s49 offen
	buffer_load_dword v171, v1, s[20:23], s49 offen
	buffer_load_dword v171, v1, s[20:23], s49 offen
	s_mov_b32 s54, 0
	s_add_i32 s60, s48, 0xa800
	s_add_i32 s61, s49, 0xc000
	s_mov_b32 s62, s49
	s_waitcnt lgkmcnt(0)
.Lrec_loop:
	s_waitcnt vmcnt(42)
	v_cvt_pk_f16_f32 v146, v2, v3
	v_cvt_pk_f16_f32 v147, v4, v5
	v_cvt_pk_f16_f32 v148, v6, v7
	v_cvt_pk_f16_f32 v149, v8, v9
	v_cvt_pk_f16_f32 v150, v10, v11
	v_cvt_pk_f16_f32 v151, v12, v13
	v_cvt_pk_f16_f32 v152, v14, v15
	v_cvt_pk_f16_f32 v153, v16, v17
	v_mul_f32_e32 v2, s40, v2
	v_mul_f32_e32 v3, s40, v3
	v_mfma_f32_32x32x16_f16 v[50:65], a[0:3], v[146:149], v[114:129]
	v_mul_f32_e32 v4, s40, v4
	v_mul_f32_e32 v5, s40, v5
	v_mul_f32_e32 v6, s40, v6
	v_mul_f32_e32 v7, s40, v7
	v_mfma_f32_32x32x16_f16 v[66:81], a[4:7], v[146:149], v[130:145]
	v_mul_f32_e32 v8, s40, v8
	v_mul_f32_e32 v9, s40, v9
	v_mul_f32_e32 v10, s40, v10
	v_mul_f32_e32 v11, s40, v11
	v_mfma_f32_32x32x16_f16 v[82:97], a[8:11], v[146:149], 0
	v_mul_f32_e32 v12, s40, v12
	v_mul_f32_e32 v13, s40, v13
	v_mul_f32_e32 v14, s40, v14
	v_mul_f32_e32 v15, s40, v15
	v_mfma_f32_32x32x16_f16 v[98:113], a[12:15], v[146:149], 0
	v_mul_f32_e32 v16, s40, v16
	v_mul_f32_e32 v17, s40, v17
	s_add_i32 s56, s60, 0
	buffer_load_dwordx4 a[0:3], v1, s[16:19], s56 offen
	s_add_i32 s57, s60, 6144
	buffer_load_dwordx4 a[4:7], v1, s[16:19], s57 offen
	s_add_i32 s56, s60, 12288
	buffer_load_dwordx4 a[8:11], v1, s[16:19], s56 offen
	s_add_i32 s57, s60, 18432
	buffer_load_dwordx4 a[12:15], v1, s[16:19], s57 offen
	s_waitcnt vmcnt(54)
	v_mfma_f32_32x32x16_f16 v[50:65], a[16:19], v[150:153], v[50:65]
	v_mfma_f32_32x32x16_f16 v[66:81], a[20:23], v[150:153], v[66:81]
	v_mfma_f32_32x32x16_f16 v[82:97], a[24:27], v[150:153], v[82:97]
	v_mfma_f32_32x32x16_f16 v[98:113], a[28:31], v[150:153], v[98:113]
	s_add_i32 s56, s60, 1024
	buffer_load_dwordx4 a[16:19], v1, s[16:19], s56 offen
	s_add_i32 s57, s60, 7168
	buffer_load_dwordx4 a[20:23], v1, s[16:19], s57 offen
	s_add_i32 s56, s60, 13312
	buffer_load_dwordx4 a[24:27], v1, s[16:19], s56 offen
	s_add_i32 s57, s60, 19456
	buffer_load_dwordx4 a[28:31], v1, s[16:19], s57 offen
	s_add_i32 s58, s61, 0
	buffer_load_dwordx4 v[114:117], v1, s[20:23], s58 offen
	s_add_i32 s59, s61, 1024
	buffer_load_dwordx4 v[118:121], v1, s[20:23], s59 offen
	s_add_i32 s58, s61, 2048
	buffer_load_dwordx4 v[122:125], v1, s[20:23], s58 offen
	s_add_i32 s59, s61, 3072
	buffer_load_dwordx4 v[126:129], v1, s[20:23], s59 offen
	s_add_i32 s58, s61, 4096
	buffer_load_dwordx4 v[130:133], v1, s[20:23], s58 offen
	s_add_i32 s59, s61, 5120
	buffer_load_dwordx4 v[134:137], v1, s[20:23], s59 offen
	s_add_i32 s58, s61, 6144
	buffer_load_dwordx4 v[138:141], v1, s[20:23], s58 offen
	s_add_i32 s59, s61, 7168
	buffer_load_dwordx4 v[142:145], v1, s[20:23], s59 offen
	s_waitcnt vmcnt(54)
	v_cvt_pk_f16_f32 v146, v18, v19
	v_cvt_pk_f16_f32 v147, v20, v21
	v_cvt_pk_f16_f32 v148, v22, v23
	v_cvt_pk_f16_f32 v149, v24, v25
	v_cvt_pk_f16_f32 v150, v26, v27
	v_cvt_pk_f16_f32 v151, v28, v29
	v_cvt_pk_f16_f32 v152, v30, v31
	v_cvt_pk_f16_f32 v153, v32, v33
	v_mul_f32_e32 v18, s40, v18
	v_mul_f32_e32 v19, s40, v19
	v_mfma_f32_32x32x16_f16 v[50:65], a[32:35], v[146:149], v[50:65]
	v_mul_f32_e32 v20, s40, v20
	v_mul_f32_e32 v21, s40, v21
	v_mul_f32_e32 v22, s40, v22
	v_mul_f32_e32 v23, s40, v23
	v_mfma_f32_32x32x16_f16 v[66:81], a[36:39], v[146:149], v[66:81]
	v_mul_f32_e32 v24, s40, v24
	v_mul_f32_e32 v25, s40, v25
	v_mul_f32_e32 v26, s40, v26
	v_mul_f32_e32 v27, s40, v27
	v_mfma_f32_32x32x16_f16 v[82:97], a[40:43], v[146:149], v[82:97]
	v_mul_f32_e32 v28, s40, v28
	v_mul_f32_e32 v29, s40, v29
	v_mul_f32_e32 v30, s40, v30
	v_mul_f32_e32 v31, s40, v31
	v_mfma_f32_32x32x16_f16 v[98:113], a[44:47], v[146:149], v[98:113]
	v_mul_f32_e32 v32, s40, v32
	v_mul_f32_e32 v33, s40, v33
	s_add_i32 s56, s60, 2048
	buffer_load_dwordx4 a[32:35], v1, s[16:19], s56 offen
	s_add_i32 s57, s60, 8192
	buffer_load_dwordx4 a[36:39], v1, s[16:19], s57 offen
	s_add_i32 s56, s60, 14336
	buffer_load_dwordx4 a[40:43], v1, s[16:19], s56 offen
	s_add_i32 s57, s60, 20480
	buffer_load_dwordx4 a[44:47], v1, s[16:19], s57 offen
	s_waitcnt vmcnt(54)
	v_mfma_f32_32x32x16_f16 v[50:65], a[48:51], v[150:153], v[50:65]
	v_mfma_f32_32x32x16_f16 v[66:81], a[52:55], v[150:153], v[66:81]
	v_mfma_f32_32x32x16_f16 v[82:97], a[56:59], v[150:153], v[82:97]
	v_mfma_f32_32x32x16_f16 v[98:113], a[60:63], v[150:153], v[98:113]
	s_add_i32 s56, s60, 3072
	buffer_load_dwordx4 a[48:51], v1, s[16:19], s56 offen
	s_add_i32 s57, s60, 9216
	buffer_load_dwordx4 a[52:55], v1, s[16:19], s57 offen
	s_add_i32 s56, s60, 15360
	buffer_load_dwordx4 a[56:59], v1, s[16:19], s56 offen
	s_add_i32 s57, s60, 21504
	buffer_load_dwordx4 a[60:63], v1, s[16:19], s57 offen
	s_waitcnt vmcnt(54)
	v_cvt_pk_f16_f32 v146, v34, v35
	v_cvt_pk_f16_f32 v147, v36, v37
	v_cvt_pk_f16_f32 v148, v38, v39
	v_cvt_pk_f16_f32 v149, v40, v41
	v_cvt_pk_f16_f32 v150, v42, v43
	v_cvt_pk_f16_f32 v151, v44, v45
	v_cvt_pk_f16_f32 v152, v46, v47
	v_cvt_pk_f16_f32 v153, v48, v49
	v_mul_f32_e32 v34, s40, v34
	v_mul_f32_e32 v35, s40, v35
	v_mfma_f32_32x32x16_f16 v[50:65], a[64:67], v[146:149], v[50:65]
	v_mul_f32_e32 v36, s40, v36
	v_mul_f32_e32 v37, s40, v37
	v_mul_f32_e32 v38, s40, v38
	v_mul_f32_e32 v39, s40, v39
	v_mfma_f32_32x32x16_f16 v[66:81], a[68:71], v[146:149], v[66:81]
	v_mul_f32_e32 v40, s40, v40
	v_mul_f32_e32 v41, s40, v41
	v_mul_f32_e32 v42, s40, v42
	v_mul_f32_e32 v43, s40, v43
	v_mfma_f32_32x32x16_f16 v[82:97], a[72:75], v[146:149], v[82:97]
	v_mul_f32_e32 v44, s40, v44
	v_mul_f32_e32 v45, s40, v45
	v_mul_f32_e32 v46, s40, v46
	v_mul_f32_e32 v47, s40, v47
	v_mfma_f32_32x32x16_f16 v[98:113], a[76:79], v[146:149], v[98:113]
	v_mul_f32_e32 v48, s40, v48
	v_mul_f32_e32 v49, s40, v49
	s_add_i32 s56, s60, 4096
	buffer_load_dwordx4 a[64:67], v1, s[16:19], s56 offen
	s_add_i32 s57, s60, 10240
	buffer_load_dwordx4 a[68:71], v1, s[16:19], s57 offen
	s_add_i32 s56, s60, 16384
	buffer_load_dwordx4 a[72:75], v1, s[16:19], s56 offen
	s_add_i32 s57, s60, 22528
	buffer_load_dwordx4 a[76:79], v1, s[16:19], s57 offen
	s_waitcnt vmcnt(54)
	v_mfma_f32_32x32x16_f16 v[50:65], a[80:83], v[150:153], v[50:65]
	v_mfma_f32_32x32x16_f16 v[66:81], a[84:87], v[150:153], v[66:81]
	v_mfma_f32_32x32x16_f16 v[82:97], a[88:91], v[150:153], v[82:97]
	v_mfma_f32_32x32x16_f16 v[98:113], a[92:95], v[150:153], v[98:113]
	s_add_i32 s56, s60, 5120
	buffer_load_dwordx4 a[80:83], v1, s[16:19], s56 offen
	s_add_i32 s57, s60, 11264
	buffer_load_dwordx4 a[84:87], v1, s[16:19], s57 offen
	s_add_i32 s56, s60, 17408
	buffer_load_dwordx4 a[88:91], v1, s[16:19], s56 offen
	s_add_i32 s57, s60, 23552
	buffer_load_dwordx4 a[92:95], v1, s[16:19], s57 offen
	s_waitcnt vmcnt(53)
	s_nop 0
	v_cvt_pk_f16_f32 v154, v50, v51
	v_cvt_pk_f16_f32 v155, v52, v53
	v_cvt_pk_f16_f32 v156, v54, v55
	v_cvt_pk_f16_f32 v157, v56, v57
	v_cvt_pk_f16_f32 v158, v58, v59
	v_cvt_pk_f16_f32 v159, v60, v61
	v_cvt_pk_f16_f32 v160, v62, v63
	v_cvt_pk_f16_f32 v161, v64, v65
	v_cvt_pk_f16_f32 v162, v66, v67
	v_cvt_pk_f16_f32 v163, v68, v69
	v_cvt_pk_f16_f32 v164, v70, v71
	v_cvt_pk_f16_f32 v165, v72, v73
	v_cvt_pk_f16_f32 v166, v74, v75
	v_cvt_pk_f16_f32 v167, v76, v77
	v_cvt_pk_f16_f32 v168, v78, v79
	v_cvt_pk_f16_f32 v169, v80, v81
	s_nop 1
	v_mfma_f32_32x32x16_f16 v[2:17], a[96:99], v[154:157], v[2:17]
	v_mfma_f32_32x32x16_f16 v[18:33], a[100:103], v[154:157], v[18:33]
	v_mfma_f32_32x32x16_f16 v[34:49], a[104:107], v[154:157], v[34:49]
	v_mfma_f32_32x32x16_f16 v[82:97], a[108:111], v[154:157], v[82:97]
	v_mfma_f32_32x32x16_f16 v[98:113], a[112:115], v[154:157], v[98:113]
	s_add_i32 s56, s60, 30720
	buffer_load_dwordx4 a[96:99], v1, s[16:19], s56 offen
	s_add_i32 s57, s60, 34816
	buffer_load_dwordx4 a[100:103], v1, s[16:19], s57 offen
	s_add_i32 s56, s60, 38912
	buffer_load_dwordx4 a[104:107], v1, s[16:19], s56 offen
	s_add_i32 s57, s60, 24576
	buffer_load_dwordx4 a[108:111], v1, s[16:19], s57 offen
	s_add_i32 s56, s60, 26624
	buffer_load_dwordx4 a[112:115], v1, s[16:19], s56 offen
	s_waitcnt vmcnt(53)
	v_mfma_f32_32x32x16_f16 v[2:17], a[116:119], v[158:161], v[2:17]
	v_mfma_f32_32x32x16_f16 v[18:33], a[120:123], v[158:161], v[18:33]
	v_mfma_f32_32x32x16_f16 v[34:49], a[124:127], v[158:161], v[34:49]
	v_mfma_f32_32x32x16_f16 v[82:97], a[128:131], v[158:161], v[82:97]
	v_mfma_f32_32x32x16_f16 v[98:113], a[132:135], v[158:161], v[98:113]
	s_add_i32 s56, s60, 31744
	buffer_load_dwordx4 a[116:119], v1, s[16:19], s56 offen
	s_add_i32 s57, s60, 35840
	buffer_load_dwordx4 a[120:123], v1, s[16:19], s57 offen
	s_add_i32 s56, s60, 39936
	buffer_load_dwordx4 a[124:127], v1, s[16:19], s56 offen
	s_add_i32 s57, s60, 25600
	buffer_load_dwordx4 a[128:131], v1, s[16:19], s57 offen
	s_add_i32 s56, s60, 27648
	buffer_load_dwordx4 a[132:135], v1, s[16:19], s56 offen
	s_waitcnt vmcnt(54)
	v_mfma_f32_32x32x16_f16 v[2:17], a[136:139], v[162:165], v[2:17]
	v_mfma_f32_32x32x16_f16 v[18:33], a[140:143], v[162:165], v[18:33]
	v_mfma_f32_32x32x16_f16 v[34:49], a[144:147], v[162:165], v[34:49]
	v_mfma_f32_32x32x16_f16 v[98:113], a[148:151], v[162:165], v[98:113]
	s_add_i32 s56, s60, 32768
	buffer_load_dwordx4 a[136:139], v1, s[16:19], s56 offen
	s_add_i32 s57, s60, 36864
	buffer_load_dwordx4 a[140:143], v1, s[16:19], s57 offen
	s_add_i32 s56, s60, 40960
	buffer_load_dwordx4 a[144:147], v1, s[16:19], s56 offen
	s_add_i32 s57, s60, 28672
	buffer_load_dwordx4 a[148:151], v1, s[16:19], s57 offen
	s_waitcnt vmcnt(54)
	v_mfma_f32_32x32x16_f16 v[2:17], a[152:155], v[166:169], v[2:17]
	v_mfma_f32_32x32x16_f16 v[18:33], a[156:159], v[166:169], v[18:33]
	v_mfma_f32_32x32x16_f16 v[34:49], a[160:163], v[166:169], v[34:49]
	v_mfma_f32_32x32x16_f16 v[98:113], a[164:167], v[166:169], v[98:113]
	s_add_i32 s56, s60, 33792
	buffer_load_dwordx4 a[152:155], v1, s[16:19], s56 offen
	s_add_i32 s57, s60, 37888
	buffer_load_dwordx4 a[156:159], v1, s[16:19], s57 offen
	s_add_i32 s56, s60, 41984
	buffer_load_dwordx4 a[160:163], v1, s[16:19], s56 offen
	s_add_i32 s57, s60, 29696
	buffer_load_dwordx4 a[164:167], v1, s[16:19], s57 offen
	s_nop 0
	s_add_i32 s58, s62, 0
	buffer_store_dwordx4 v[82:85], v1, s[24:27], s58 offen
	s_add_i32 s59, s62, 1024
	buffer_store_dwordx4 v[86:89], v1, s[24:27], s59 offen
	s_add_i32 s58, s62, 2048
	buffer_store_dwordx4 v[90:93], v1, s[24:27], s58 offen
	s_add_i32 s59, s62, 3072
	buffer_store_dwordx4 v[94:97], v1, s[24:27], s59 offen
	s_add_i32 s58, s62, 4096
	buffer_store_dwordx4 v[98:101], v1, s[24:27], s58 offen
	s_add_i32 s59, s62, 5120
	buffer_store_dwordx4 v[102:105], v1, s[24:27], s59 offen
	s_add_i32 s58, s62, 6144
	buffer_store_dwordx4 v[106:109], v1, s[24:27], s58 offen
	s_add_i32 s59, s62, 7168
	buffer_store_dwordx4 v[110:113], v1, s[24:27], s59 offen
	s_add_i32 s54, s54, 1
	s_add_i32 s56, s54, 1
	s_min_i32 s56, s56, 7
	s_mul_i32 s60, s56, 0xa800
	s_add_i32 s60, s60, s48
	s_mul_i32 s61, s56, 0xc000
	s_add_i32 s61, s61, s49
	s_add_i32 s62, s62, 0xc000
	s_mov_b32 s40, s41
	s_mov_b32 s41, s42
	s_mov_b32 s42, s43
	s_mov_b32 s43, s44
	s_mov_b32 s44, s45
	s_mov_b32 s45, s46
	s_mov_b32 s46, s47
	s_cmp_lt_u32 s54, 8
	s_cbranch_scc1 .Lrec_loop
	s_nop 7
	s_add_i32 s56, s50, 0
	buffer_store_dword v2, v170, s[32:35], s56 offen
	buffer_store_dword v3, v170, s[32:35], s56 offen offset:768
	buffer_store_dword v4, v170, s[32:35], s56 offen offset:1536
	buffer_store_dword v5, v170, s[32:35], s56 offen offset:2304
	s_add_i32 s56, s50, 6144
	buffer_store_dword v6, v170, s[32:35], s56 offen
	buffer_store_dword v7, v170, s[32:35], s56 offen offset:768
	buffer_store_dword v8, v170, s[32:35], s56 offen offset:1536
	buffer_store_dword v9, v170, s[32:35], s56 offen offset:2304
	s_add_i32 s56, s50, 12288
	buffer_store_dword v10, v170, s[32:35], s56 offen
	buffer_store_dword v11, v170, s[32:35], s56 offen offset:768
	buffer_store_dword v12, v170, s[32:35], s56 offen offset:1536
	buffer_store_dword v13, v170, s[32:35], s56 offen offset:2304
	s_add_i32 s56, s50, 18432
	buffer_store_dword v14, v170, s[32:35], s56 offen
	buffer_store_dword v15, v170, s[32:35], s56 offen offset:768
	buffer_store_dword v16, v170, s[32:35], s56 offen offset:1536
	buffer_store_dword v17, v170, s[32:35], s56 offen offset:2304
	s_add_i32 s56, s50, 24576
	buffer_store_dword v18, v170, s[32:35], s56 offen
	buffer_store_dword v19, v170, s[32:35], s56 offen offset:768
	buffer_store_dword v20, v170, s[32:35], s56 offen offset:1536
	buffer_store_dword v21, v170, s[32:35], s56 offen offset:2304
	s_add_i32 s56, s50, 30720
	buffer_store_dword v22, v170, s[32:35], s56 offen
	buffer_store_dword v23, v170, s[32:35], s56 offen offset:768
	buffer_store_dword v24, v170, s[32:35], s56 offen offset:1536
	buffer_store_dword v25, v170, s[32:35], s56 offen offset:2304
	s_add_i32 s56, s50, 36864
	buffer_store_dword v26, v170, s[32:35], s56 offen
	buffer_store_dword v27, v170, s[32:35], s56 offen offset:768
	buffer_store_dword v28, v170, s[32:35], s56 offen offset:1536
	buffer_store_dword v29, v170, s[32:35], s56 offen offset:2304
	s_add_i32 s56, s50, 43008
	buffer_store_dword v30, v170, s[32:35], s56 offen
	buffer_store_dword v31, v170, s[32:35], s56 offen offset:768
	buffer_store_dword v32, v170, s[32:35], s56 offen offset:1536
	buffer_store_dword v33, v170, s[32:35], s56 offen offset:2304
	s_add_i32 s56, s50, 49152
	buffer_store_dword v34, v170, s[32:35], s56 offen
	buffer_store_dword v35, v170, s[32:35], s56 offen offset:768
	buffer_store_dword v36, v170, s[32:35], s56 offen offset:1536
	buffer_store_dword v37, v170, s[32:35], s56 offen offset:2304
	s_add_i32 s56, s50, 55296
	buffer_store_dword v38, v170, s[32:35], s56 offen
	buffer_store_dword v39, v170, s[32:35], s56 offen offset:768
	buffer_store_dword v40, v170, s[32:35], s56 offen offset:1536
	buffer_store_dword v41, v170, s[32:35], s56 offen offset:2304
	s_add_i32 s56, s50, 61440
	buffer_store_dword v42, v170, s[32:35], s56 offen
	buffer_store_dword v43, v170, s[32:35], s56 offen offset:768
	buffer_store_dword v44, v170, s[32:35], s56 offen offset:1536
	buffer_store_dword v45, v170, s[32:35], s56 offen offset:2304
	s_add_i32 s56, s50, 67584
	buffer_store_dword v46, v170, s[32:35], s56 offen
	buffer_store_dword v47, v170, s[32:35], s56 offen offset:768
	buffer_store_dword v48, v170, s[32:35], s56 offen offset:1536
	buffer_store_dword v49, v170, s[32:35], s56 offen offset:2304
	s_endpgm

	.amdhsa_kernel _Z16rec_chunk_kernelPKDF16_PKfS2_S2_PfS3_
		.amdhsa_group_segment_fixed_size 0
		.amdhsa_private_segment_fixed_size 0
		.amdhsa_kernarg_size 48
		.amdhsa_user_sgpr_count 2
		.amdhsa_user_sgpr_dispatch_ptr 0
		.amdhsa_user_sgpr_queue_ptr 0
		.amdhsa_user_sgpr_kernarg_segment_ptr 1
		.amdhsa_user_sgpr_dispatch_id 0
		.amdhsa_user_sgpr_kernarg_preload_length 0
		.amdhsa_user_sgpr_kernarg_preload_offset 0
		.amdhsa_user_sgpr_private_segment_size 0
		.amdhsa_uses_dynamic_stack 0
		.amdhsa_enable_private_segment 0
		.amdhsa_system_sgpr_workgroup_id_x 1
		.amdhsa_system_sgpr_workgroup_id_y 0
		.amdhsa_system_sgpr_workgroup_id_z 0
		.amdhsa_system_sgpr_workgroup_info 0
		.amdhsa_system_vgpr_workitem_id 0
		.amdhsa_next_free_vgpr 424
		.amdhsa_next_free_sgpr 96
		.amdhsa_accum_offset 256
		.amdhsa_reserve_vcc 1
		.amdhsa_float_round_mode_32 0
		.amdhsa_float_round_mode_16_64 0
		.amdhsa_float_denorm_mode_32 3
		.amdhsa_float_denorm_mode_16_64 3
		.amdhsa_dx10_clamp 1
		.amdhsa_ieee_mode 1
		.amdhsa_fp16_overflow 0
		.amdhsa_tg_split 0
		.amdhsa_exception_fp_ieee_invalid_op 0
		.amdhsa_exception_fp_denorm_src 0
		.amdhsa_exception_fp_ieee_div_zero 0
		.amdhsa_exception_fp_ieee_overflow 0
		.amdhsa_exception_fp_ieee_underflow 0
		.amdhsa_exception_fp_ieee_inexact 0
		.amdhsa_exception_int_div_zero 0
	.end_amdhsa_kernel

amdhsa.kernels:
  - .agpr_count:     0
    .args:
      - .offset:         0
        .size:           88
        .value_kind:     by_value
    .group_segment_fixed_size: 16640
    .kernarg_segment_align: 8
    .kernarg_segment_size: 88
    .language:       OpenCL C
    .language_version:
      - 2
      - 0
    .max_flat_workgroup_size: 256
    .name:           _Z15prologue_kernel7ProArgs
    .private_segment_fixed_size: 0
    .sgpr_count:     28
    .sgpr_spill_count: 0
    .symbol:         _Z15prologue_kernel7ProArgs.kd
    .uniform_work_group_size: 1
    .uses_dynamic_stack: false
    .vgpr_count:     54
    .vgpr_spill_count: 0
    .wavefront_size: 64
  - .agpr_count:     0
    .args:
      - .offset:         0
        .size:           96
        .value_kind:     by_value
    .group_segment_fixed_size: 149760
    .kernarg_segment_align: 8
    .kernarg_segment_size: 96
    .language:       OpenCL C
    .language_version:
      - 2
      - 0
    .max_flat_workgroup_size: 384
    .name:           _Z11prep_kernel8PrepArgs
    .private_segment_fixed_size: 0
    .sgpr_count:     41
    .sgpr_spill_count: 0
    .symbol:         _Z11prep_kernel8PrepArgs.kd
    .uniform_work_group_size: 1
    .uses_dynamic_stack: false
    .vgpr_count:     256
    .vgpr_spill_count: 0
    .wavefront_size: 64
  - .agpr_count:     168
    .args:
      - .actual_access:  read_only
        .address_space:  global
        .offset:         0
        .size:           8
        .value_kind:     global_buffer
      - .actual_access:  read_only
        .address_space:  global
        .offset:         8
        .size:           8
        .value_kind:     global_buffer
      - .actual_access:  read_only
        .address_space:  global
        .offset:         16
        .size:           8
        .value_kind:     global_buffer
      - .actual_access:  read_only
        .address_space:  global
        .offset:         24
        .size:           8
        .value_kind:     global_buffer
      - .actual_access:  write_only
        .address_space:  global
        .offset:         32
        .size:           8
        .value_kind:     global_buffer
      - .actual_access:  write_only
        .address_space:  global
        .offset:         40
        .size:           8
        .value_kind:     global_buffer
    .group_segment_fixed_size: 0
    .kernarg_segment_align: 8
    .kernarg_segment_size: 48
    .language:       OpenCL C
    .language_version:
      - 2
      - 0
    .max_flat_workgroup_size: 64
    .name:           _Z16rec_chunk_kernelPKDF16_PKfS2_S2_PfS3_
    .private_segment_fixed_size: 0
    .sgpr_count:     42
    .sgpr_spill_count: 0
    .symbol:         _Z16rec_chunk_kernelPKDF16_PKfS2_S2_PfS3_.kd
    .uniform_work_group_size: 1
    .uses_dynamic_stack: false
    .vgpr_count:     424
    .vgpr_spill_count: 0
    .wavefront_size: 64
  - .agpr_count:     0
    .args:
      - .actual_access:  read_only
        .address_space:  global
        .offset:         0
        .size:           8
        .value_kind:     global_buffer
      - .actual_access:  read_only
        .address_space:  global
        .offset:         8
        .size:           8
        .value_kind:     global_buffer
      - .actual_access:  read_only
        .address_space:  global
        .offset:         16
        .size:           8
        .value_kind:     global_buffer
      - .actual_access:  write_only
        .address_space:  global
        .offset:         24
        .size:           8
        .value_kind:     global_buffer
      - .actual_access:  read_only
        .address_space:  global
        .offset:         32
        .size:           8
        .value_kind:     global_buffer
      - .actual_access:  write_only
        .address_space:  global
        .offset:         40
        .size:           8
        .value_kind:     global_buffer
    .group_segment_fixed_size: 16640
    .kernarg_segment_align: 8
    .kernarg_segment_size: 48
    .language:       OpenCL C
    .language_version:
      - 2
      - 0
    .max_flat_workgroup_size: 256
    .name:           _Z16norm_gate_kernelPKfPKDF16_S0_PDF16_S0_S3_
    .private_segment_fixed_size: 0
    .sgpr_count:     20
    .sgpr_spill_count: 0
    .symbol:         _Z16norm_gate_kernelPKfPKDF16_S0_PDF16_S0_S3_.kd
    .uniform_work_group_size: 1
    .uses_dynamic_stack: false
    .vgpr_count:     63
    .vgpr_spill_count: 0
    .wavefront_size: 64
  - .agpr_count:     0
    .args:
      - .address_space:  global
        .offset:         0
        .size:           8
        .value_kind:     global_buffer
      - .address_space:  global
        .offset:         8
        .size:           8
        .value_kind:     global_buffer
      - .actual_access:  write_only
        .address_space:  global
        .offset:         16
        .size:           8
        .value_kind:     global_buffer
      - .offset:         24
        .size:           4
        .value_kind:     by_value
      - .offset:         28
        .size:           4
        .value_kind:     by_value
      - .offset:         32
        .size:           4
        .value_kind:     by_value
      - .offset:         36
        .size:           4
        .value_kind:     by_value
    .group_segment_fixed_size: 159744
    .kernarg_segment_align: 8
    .kernarg_segment_size: 40
    .language:       OpenCL C
    .language_version:
      - 2
      - 0
    .max_flat_workgroup_size: 512
    .name:           _Z8gemm_f16ILi256ELi160ELi4ELi2ELi2ELi1ELi1EEvPKDF16_S1_Pviiii
    .private_segment_fixed_size: 0
    .sgpr_count:     22
    .sgpr_spill_count: 0
    .symbol:         _Z8gemm_f16ILi256ELi160ELi4ELi2ELi2ELi1ELi1EEvPKDF16_S1_Pviiii.kd
    .uniform_work_group_size: 1
    .uses_dynamic_stack: false
    .vgpr_count:     172
    .vgpr_spill_count: 0
    .wavefront_size: 64
  - .agpr_count:     32
    .args:
      - .address_space:  global
        .offset:         0
        .size:           8
        .value_kind:     global_buffer
      - .address_space:  global
        .offset:         8
        .size:           8
        .value_kind:     global_buffer
      - .actual_access:  write_only
        .address_space:  global
        .offset:         16
        .size:           8
        .value_kind:     global_buffer
      - .offset:         24
        .size:           4
        .value_kind:     by_value
      - .offset:         28
        .size:           4
        .value_kind:     by_value
      - .offset:         32
        .size:           4
        .value_kind:     by_value
      - .offset:         36
        .size:           4
        .value_kind:     by_value
    .group_segment_fixed_size: 98304
    .kernarg_segment_align: 8
    .kernarg_segment_size: 40
    .language:       OpenCL C
    .language_version:
      - 2
      - 0
    .max_flat_workgroup_size: 256
    .name:           _Z8gemm_f16ILi128ELi64ELi2ELi2ELi4ELi2ELi0EEvPKDF16_S1_Pviiii
    .private_segment_fixed_size: 0
    .sgpr_count:     25
    .sgpr_spill_count: 0
    .symbol:         _Z8gemm_f16ILi128ELi64ELi2ELi2ELi4ELi2ELi0EEvPKDF16_S1_Pviiii.kd
    .uniform_work_group_size: 1
    .uses_dynamic_stack: false
    .vgpr_count:     96
    .vgpr_spill_count: 0
    .wavefront_size: 64
